# P7b EpiOut epilogue: hoist the 32 serialized x loads into a 12-deep VGPR ring with counted vmcnt
# speedup vs baseline: 1.0049x; 1.0049x over previous
; #define LAS __attribute__((address_space(3)))
; DI unsigned pk2(float lo, float hi) { f32x2 v = {lo, hi}; bf16x2_t b = __builtin_convertvector(v, bf16x2_t); return __builtin_bit_cast(unsigned, b); }
;     DI void operator()(const f32x4 (&acc)[2][2][4][2], const Unit& u, int wr, int wc, int fr, int fq, const LAS unsigned char* slot) const {
;         int zz = 0; asm volatile("" : "+v"(zz));
;         const int row0 = u.pm * BM + wr * 64 + fr + zz, col0 = u.pn * BM + wc * 32 + 4 * fq;
;         f32x4 mv[2][2];
; #pragma unroll
;         for (int bj = 0; bj < 2; ++bj)
; #pragma unroll
;             for (int n = 0; n < 2; ++n) { const int lc = bj * HALF + wc * 32 + n * 16 + 4 * fq; mv[bj][n] = *(const LAS f32x4*)(slot + 1024 + 4 * lc) * *(const LAS f32x4*)(slot + 2048 + 4 * lc); }
; #pragma unroll
;         for (int ai = 0; ai < 2; ++ai)
; #pragma unroll
;             for (int m = 0; m < 4; ++m) { const size_t off = (size_t)(row0 + ai * HALF + m * 16) * D + col0; const float rs = *(const LAS float*)(slot + 4 * (ai * HALF + wr * 64 + m * 16 + fr));
; #pragma unroll
;                 for (int bj = 0; bj < 2; ++bj)
; #pragma unroll
;                     for (int n = 0; n < 2; ++n) { const f32x4 xv = *(const f32x4*)(x + off + bj * HALF + n * 16); const i32x4 ia = __builtin_bit_cast(i32x4, acc[ai][bj][m][n]);
;                         const f32x4 af = {(float)ia[0], (float)ia[1], (float)ia[2], (float)ia[3]};
;                         const f32x4 r = xv + (mv[bj][n] * rs) * af; *(u32x2*)(X1 + off + bj * HALF + n * 16) = (u32x2){pk2(r[0], r[1]), pk2(r[2], r[3])}; } }
.LBB0_1656:
	v_mov_b32_e32 v134, v135
	s_lshl_b32 s54, s79, 8
	v_lshl_or_b32 v144, s78, 8, v157
	v_add3_u32 v142, s54, v154, v134
	v_ashrrev_i32_e32 v143, 31, v142
	v_ashrrev_i32_e32 v145, 31, v144
	v_lshlrev_b64 v[142:143], 11, v[142:143]
	v_lshl_add_u64 v[142:143], v[142:143], 0, v[144:145]
	v_lshl_add_u64 v[182:183], v[142:143], 2, s[10:11]
	v_lshl_add_u64 v[240:241], v[142:143], 0, s[28:29]
	v_lshl_add_u64 v[242:243], v[142:143], 0, s[30:31]
	v_lshl_add_u64 v[244:245], v[142:143], 0, s[34:35]
	v_lshl_add_u64 v[246:247], v[142:143], 0, s[16:17]
	v_lshl_add_u64 v[248:249], v[142:143], 0, s[36:37]
	v_lshl_add_u64 v[250:251], v[142:143], 0, s[38:39]
	v_lshl_add_u64 v[252:253], v[142:143], 0, s[42:43]
	v_lshl_add_u64 v[240:241], v[240:241], 2, s[10:11]
	v_lshl_add_u64 v[242:243], v[242:243], 2, s[10:11]
	v_lshl_add_u64 v[244:245], v[244:245], 2, s[10:11]
	v_lshl_add_u64 v[246:247], v[246:247], 2, s[10:11]
	v_lshl_add_u64 v[248:249], v[248:249], 2, s[10:11]
	v_lshl_add_u64 v[250:251], v[250:251], 2, s[10:11]
	v_lshl_add_u64 v[252:253], v[252:253], 2, s[10:11]
	global_load_dwordx4 v[192:195], v[182:183], off
	global_load_dwordx4 v[196:199], v[182:183], off offset:64
	global_load_dwordx4 v[200:203], v[182:183], off offset:512
	global_load_dwordx4 v[204:207], v[182:183], off offset:576
	global_load_dwordx4 v[208:211], v[240:241], off
	global_load_dwordx4 v[212:215], v[240:241], off offset:64
	global_load_dwordx4 v[216:219], v[240:241], off offset:512
	global_load_dwordx4 v[220:223], v[240:241], off offset:576
	global_load_dwordx4 v[224:227], v[242:243], off
	global_load_dwordx4 v[228:231], v[242:243], off offset:64
	global_load_dwordx4 v[232:235], v[242:243], off offset:512
	global_load_dwordx4 v[236:239], v[242:243], off offset:576
	s_lshl_b32 s54, s74, 12
	s_and_b32 s54, s54, 0x1000
	s_add_i32 s54, s54, 0
	s_add_i32 s54, s54, 0x21000
	v_add_u32_e32 v169, s54, v158
	v_add_u32_e32 v134, s54, v155
	ds_read_b128 v[148:151], v169 offset:2048
	ds_read_b128 v[170:173], v169 offset:1024
	ds_read_b128 v[174:177], v169 offset:1088
	ds_read2_b32 v[188:189], v134 offset1:16
	ds_read_b128 v[178:181], v169 offset:2112
	v_cvt_f32_i32_e32 v185, v127
	v_cvt_f32_i32_e32 v184, v126
	v_cvt_f32_i32_e32 v187, v129
	v_cvt_f32_i32_e32 v186, v128
	s_waitcnt lgkmcnt(0)
	v_pk_mul_f32 v[126:127], v[172:173], v[150:151]
	v_pk_mul_f32 v[128:129], v[170:171], v[148:149]
	v_pk_mul_f32 v[148:149], v[126:127], v[188:189] op_sel_hi:[1,0]
	v_pk_mul_f32 v[150:151], v[128:129], v[188:189] op_sel_hi:[1,0]
	v_lshl_add_u64 v[190:191], v[142:143], 1, s[20:21]
	v_cvt_f32_i32_e32 v111, v111
	v_cvt_f32_i32_e32 v110, v110
	v_cvt_f32_i32_e32 v113, v113
	v_cvt_f32_i32_e32 v112, v112
	v_cvt_f32_i32_e32 v107, v107
	v_cvt_f32_i32_e32 v109, v109
	v_cvt_f32_i32_e32 v108, v108
	v_cvt_f32_i32_e32 v106, v106
	v_cvt_f32_i32_e32 v103, v103
	v_cvt_f32_i32_e32 v105, v105
	v_cvt_f32_i32_e32 v104, v104
	v_cvt_f32_i32_e32 v102, v102
	v_cvt_f32_i32_e32 v99, v99
	v_cvt_f32_i32_e32 v98, v98
	v_cvt_f32_i32_e32 v101, v101
	v_cvt_f32_i32_e32 v100, v100
	v_cvt_f32_i32_e32 v95, v95
	v_cvt_f32_i32_e32 v94, v94
	v_cvt_f32_i32_e32 v97, v97
	v_cvt_f32_i32_e32 v96, v96
	v_cvt_f32_i32_e32 v91, v91
	v_cvt_f32_i32_e32 v93, v93
	v_cvt_f32_i32_e32 v92, v92
	v_cvt_f32_i32_e32 v90, v90
	v_cvt_f32_i32_e32 v87, v87
	v_cvt_f32_i32_e32 v89, v89
	v_cvt_f32_i32_e32 v88, v88
	v_cvt_f32_i32_e32 v86, v86
	v_cvt_f32_i32_e32 v83, v83
	v_cvt_f32_i32_e32 v82, v82
	v_cvt_f32_i32_e32 v85, v85
	v_cvt_f32_i32_e32 v84, v84
	v_cvt_f32_i32_e32 v79, v79
	v_cvt_f32_i32_e32 v78, v78
	v_cvt_f32_i32_e32 v81, v81
	v_cvt_f32_i32_e32 v80, v80
	v_cvt_f32_i32_e32 v75, v75
	v_cvt_f32_i32_e32 v77, v77
	v_cvt_f32_i32_e32 v76, v76
	v_cvt_f32_i32_e32 v74, v74
	v_cvt_f32_i32_e32 v71, v71
	v_cvt_f32_i32_e32 v73, v73
	v_cvt_f32_i32_e32 v72, v72
	v_cvt_f32_i32_e32 v70, v70
	v_cvt_f32_i32_e32 v67, v67
	v_cvt_f32_i32_e32 v66, v66
	v_cvt_f32_i32_e32 v69, v69
	v_cvt_f32_i32_e32 v68, v68
	v_cvt_f32_i32_e32 v63, v63
	v_cvt_f32_i32_e32 v62, v62
	v_cvt_f32_i32_e32 v65, v65
	v_cvt_f32_i32_e32 v64, v64
	v_cvt_f32_i32_e32 v59, v59
	v_cvt_f32_i32_e32 v61, v61
	v_cvt_f32_i32_e32 v60, v60
	v_cvt_f32_i32_e32 v58, v58
	v_cvt_f32_i32_e32 v55, v55
	v_cvt_f32_i32_e32 v57, v57
	v_cvt_f32_i32_e32 v56, v56
	v_cvt_f32_i32_e32 v54, v54
	v_cvt_f32_i32_e32 v51, v51
	v_cvt_f32_i32_e32 v50, v50
	v_cvt_f32_i32_e32 v53, v53
	s_waitcnt vmcnt(11)
	v_pk_fma_f32 v[146:147], v[148:149], v[186:187], v[194:195]
	v_pk_fma_f32 v[144:145], v[150:151], v[184:185], v[192:193]
	v_cvt_f32_i32_e32 v149, v123
	v_cvt_pk_bf16_f32 v144, v144, v145
	v_cvt_pk_bf16_f32 v145, v146, v147
	global_store_dwordx2 v[190:191], v[144:145], off
	global_load_dwordx4 v[192:195], v[244:245], off
	v_cvt_f32_i32_e32 v148, v122
	v_cvt_f32_i32_e32 v151, v125
	v_cvt_f32_i32_e32 v150, v124
	v_pk_mul_f32 v[122:123], v[176:177], v[180:181]
	v_pk_mul_f32 v[124:125], v[174:175], v[178:179]
	v_pk_mul_f32 v[170:171], v[122:123], v[188:189] op_sel_hi:[1,0]
	v_pk_mul_f32 v[172:173], v[124:125], v[188:189] op_sel_hi:[1,0]
	v_cvt_f32_i32_e32 v185, v119
	v_cvt_f32_i32_e32 v184, v118
	v_cvt_f32_i32_e32 v187, v121
	v_cvt_f32_i32_e32 v186, v120
	v_cvt_f32_i32_e32 v52, v52
	v_cvt_f32_i32_e32 v47, v47
	v_cvt_f32_i32_e32 v46, v46
	v_cvt_f32_i32_e32 v49, v49
	v_cvt_f32_i32_e32 v48, v48
	v_cvt_f32_i32_e32 v43, v43
	v_cvt_f32_i32_e32 v45, v45
	v_cvt_f32_i32_e32 v44, v44
	v_cvt_f32_i32_e32 v42, v42
	v_cvt_f32_i32_e32 v35, v35
	v_cvt_f32_i32_e32 v37, v37
	v_cvt_f32_i32_e32 v36, v36
	v_cvt_f32_i32_e32 v34, v34
	v_cvt_f32_i32_e32 v23, v23
	v_cvt_f32_i32_e32 v22, v22
	v_cvt_f32_i32_e32 v25, v25
	v_cvt_f32_i32_e32 v24, v24
	v_cvt_f32_i32_e32 v27, v27
	v_cvt_f32_i32_e32 v26, v26
	v_cvt_f32_i32_e32 v29, v29
	v_cvt_f32_i32_e32 v28, v28
	v_cvt_f32_i32_e32 v19, v19
	v_cvt_f32_i32_e32 v21, v21
	v_cvt_f32_i32_e32 v20, v20
	v_cvt_f32_i32_e32 v18, v18
	v_cvt_f32_i32_e32 v7, v7
	v_cvt_f32_i32_e32 v6, v6
	v_cvt_f32_i32_e32 v9, v9
	v_cvt_f32_i32_e32 v8, v8
	v_cvt_f32_i32_e32 v3, v3
	v_cvt_f32_i32_e32 v5, v5
	v_cvt_f32_i32_e32 v4, v4
	v_cvt_f32_i32_e32 v2, v2
	s_and_b64 vcc, exec, s[4:5]
	s_mov_b64 s[4:5], -1
	s_waitcnt vmcnt(12)
; #define LAS __attribute__((address_space(3)))
; DI unsigned pk2(float lo, float hi) { f32x2 v = {lo, hi}; bf16x2_t b = __builtin_convertvector(v, bf16x2_t); return __builtin_bit_cast(unsigned, b); }
;     DI void operator()(const f32x4 (&acc)[2][2][4][2], const Unit& u, int wr, int wc, int fr, int fq, const LAS unsigned char* slot) const {
;     ...
;         for (int ai = 0; ai < 2; ++ai)
; #pragma unroll
;             for (int m = 0; m < 4; ++m) { const size_t off = (size_t)(row0 + ai * HALF + m * 16) * D + col0; const float rs = *(const LAS float*)(slot + 4 * (ai * HALF + wr * 64 + m * 16 + fr));
; #pragma unroll
;                 for (int bj = 0; bj < 2; ++bj)
; #pragma unroll
;                     for (int n = 0; n < 2; ++n) { const f32x4 xv = *(const f32x4*)(x + off + bj * HALF + n * 16); const i32x4 ia = __builtin_bit_cast(i32x4, acc[ai][bj][m][n]);
;                         const f32x4 af = {(float)ia[0], (float)ia[1], (float)ia[2], (float)ia[3]};
;                         const f32x4 r = xv + (mv[bj][n] * rs) * af; *(u32x2*)(X1 + off + bj * HALF + n * 16) = (u32x2){pk2(r[0], r[1]), pk2(r[2], r[3])}; } }
	v_pk_fma_f32 v[146:147], v[170:171], v[150:151], v[198:199]
	v_pk_fma_f32 v[144:145], v[172:173], v[148:149], v[196:197]
	s_nop 0
	v_cvt_pk_bf16_f32 v144, v144, v145
	v_cvt_pk_bf16_f32 v145, v146, v147
	global_store_dwordx2 v[190:191], v[144:145], off offset:32
	global_load_dwordx4 v[196:199], v[244:245], off offset:64
	ds_read_b128 v[148:151], v169 offset:1536
	ds_read_b128 v[170:173], v169 offset:2560
	ds_read_b128 v[174:177], v169 offset:1600
	ds_read_b128 v[178:181], v169 offset:2624
	s_waitcnt lgkmcnt(2)
	v_pk_mul_f32 v[118:119], v[150:151], v[172:173]
	v_pk_mul_f32 v[120:121], v[148:149], v[170:171]
	v_pk_mul_f32 v[148:149], v[118:119], v[188:189] op_sel_hi:[1,0]
	v_pk_mul_f32 v[150:151], v[120:121], v[188:189] op_sel_hi:[1,0]
	v_lshl_add_u64 v[170:171], v[142:143], 0, s[28:29]
	v_lshl_add_u64 v[172:173], v[170:171], 2, s[10:11]
	s_waitcnt vmcnt(13)
	v_pk_fma_f32 v[146:147], v[148:149], v[186:187], v[202:203]
	v_pk_fma_f32 v[144:145], v[150:151], v[184:185], v[200:201]
	v_cvt_f32_i32_e32 v149, v115
	v_cvt_pk_bf16_f32 v144, v144, v145
	v_cvt_pk_bf16_f32 v145, v146, v147
	global_store_dwordx2 v[190:191], v[144:145], off offset:256
	global_load_dwordx4 v[200:203], v[244:245], off offset:512
	v_cvt_f32_i32_e32 v148, v114
	v_cvt_f32_i32_e32 v151, v117
	v_cvt_f32_i32_e32 v150, v116
	s_waitcnt lgkmcnt(0)
	v_pk_mul_f32 v[114:115], v[176:177], v[180:181]
	v_pk_mul_f32 v[116:117], v[174:175], v[178:179]
	v_pk_mul_f32 v[174:175], v[114:115], v[188:189] op_sel_hi:[1,0]
	v_pk_mul_f32 v[176:177], v[116:117], v[188:189] op_sel_hi:[1,0]
	s_waitcnt vmcnt(14)
	v_pk_fma_f32 v[146:147], v[174:175], v[150:151], v[206:207]
	v_pk_fma_f32 v[144:145], v[176:177], v[148:149], v[204:205]
	v_mov_b32_e32 v150, v189
	v_cvt_pk_bf16_f32 v144, v144, v145
	v_cvt_pk_bf16_f32 v145, v146, v147
	global_store_dwordx2 v[190:191], v[144:145], off offset:288
	global_load_dwordx4 v[204:207], v[244:245], off offset:576
	v_lshl_add_u64 v[148:149], v[170:171], 1, s[20:21]
	v_pk_mul_f32 v[170:171], v[126:127], v[150:151] op_sel_hi:[1,0]
	v_pk_mul_f32 v[174:175], v[128:129], v[150:151] op_sel_hi:[1,0]
	s_waitcnt vmcnt(15)
	v_pk_fma_f32 v[112:113], v[170:171], v[112:113], v[210:211]
	v_pk_fma_f32 v[110:111], v[174:175], v[110:111], v[208:209]
	v_pk_mul_f32 v[144:145], v[122:123], v[150:151] op_sel_hi:[1,0]
	v_cvt_pk_bf16_f32 v110, v110, v111
	v_cvt_pk_bf16_f32 v111, v112, v113
	global_store_dwordx2 v[148:149], v[110:111], off
	global_load_dwordx4 v[208:211], v[246:247], off
	v_pk_mul_f32 v[146:147], v[124:125], v[150:151] op_sel_hi:[1,0]
	s_waitcnt vmcnt(16)
	v_pk_fma_f32 v[108:109], v[144:145], v[108:109], v[214:215]
	v_pk_fma_f32 v[106:107], v[146:147], v[106:107], v[212:213]
	v_pk_mul_f32 v[110:111], v[118:119], v[150:151] op_sel_hi:[1,0]
	v_cvt_pk_bf16_f32 v106, v106, v107
	v_cvt_pk_bf16_f32 v107, v108, v109
	global_store_dwordx2 v[148:149], v[106:107], off offset:32
	global_load_dwordx4 v[212:215], v[246:247], off offset:64
	v_pk_mul_f32 v[112:113], v[120:121], v[150:151] op_sel_hi:[1,0]
	s_waitcnt vmcnt(17)
	v_pk_fma_f32 v[104:105], v[110:111], v[104:105], v[218:219]
	v_pk_fma_f32 v[102:103], v[112:113], v[102:103], v[216:217]
	v_pk_mul_f32 v[110:111], v[114:115], v[150:151] op_sel_hi:[1,0]
	v_cvt_pk_bf16_f32 v102, v102, v103
	v_cvt_pk_bf16_f32 v103, v104, v105
	global_store_dwordx2 v[148:149], v[102:103], off offset:256
	global_load_dwordx4 v[216:219], v[246:247], off offset:512
	v_pk_mul_f32 v[112:113], v[116:117], v[150:151] op_sel_hi:[1,0]
	v_lshl_add_u64 v[106:107], v[142:143], 0, s[30:31]
	v_lshl_add_u64 v[108:109], v[106:107], 2, s[10:11]
	s_waitcnt vmcnt(18)
	v_pk_fma_f32 v[100:101], v[110:111], v[100:101], v[222:223]
	v_pk_fma_f32 v[98:99], v[112:113], v[98:99], v[220:221]
	ds_read2_b32 v[102:103], v134 offset0:32 offset1:48
	v_cvt_pk_bf16_f32 v98, v98, v99
	v_cvt_pk_bf16_f32 v99, v100, v101
	global_store_dwordx2 v[148:149], v[98:99], off offset:288
	global_load_dwordx4 v[220:223], v[246:247], off offset:576
	v_lshl_add_u64 v[104:105], v[106:107], 1, s[20:21]
	s_waitcnt lgkmcnt(0)
	v_pk_mul_f32 v[106:107], v[126:127], v[102:103] op_sel_hi:[1,0]
	v_pk_mul_f32 v[110:111], v[128:129], v[102:103] op_sel_hi:[1,0]
	s_waitcnt vmcnt(19)
	v_pk_fma_f32 v[96:97], v[106:107], v[96:97], v[226:227]
	v_pk_fma_f32 v[94:95], v[110:111], v[94:95], v[224:225]
	v_pk_mul_f32 v[98:99], v[122:123], v[102:103] op_sel_hi:[1,0]
	v_cvt_pk_bf16_f32 v94, v94, v95
	v_cvt_pk_bf16_f32 v95, v96, v97
	global_store_dwordx2 v[104:105], v[94:95], off
	global_load_dwordx4 v[224:227], v[248:249], off
	v_pk_mul_f32 v[100:101], v[124:125], v[102:103] op_sel_hi:[1,0]
	s_waitcnt vmcnt(20)
	v_pk_fma_f32 v[92:93], v[98:99], v[92:93], v[230:231]
	v_pk_fma_f32 v[90:91], v[100:101], v[90:91], v[228:229]
	v_pk_mul_f32 v[94:95], v[118:119], v[102:103] op_sel_hi:[1,0]
	v_cvt_pk_bf16_f32 v90, v90, v91
	v_cvt_pk_bf16_f32 v91, v92, v93
	global_store_dwordx2 v[104:105], v[90:91], off offset:32
	global_load_dwordx4 v[228:231], v[248:249], off offset:64
	v_pk_mul_f32 v[96:97], v[120:121], v[102:103] op_sel_hi:[1,0]
	s_waitcnt vmcnt(21)
	v_pk_fma_f32 v[88:89], v[94:95], v[88:89], v[234:235]
	v_pk_fma_f32 v[86:87], v[96:97], v[86:87], v[232:233]
	v_pk_mul_f32 v[94:95], v[114:115], v[102:103] op_sel_hi:[1,0]
	v_cvt_pk_bf16_f32 v86, v86, v87
	v_cvt_pk_bf16_f32 v87, v88, v89
	global_store_dwordx2 v[104:105], v[86:87], off offset:256
	global_load_dwordx4 v[232:235], v[248:249], off offset:512
	v_pk_mul_f32 v[96:97], v[116:117], v[102:103] op_sel_hi:[1,0]
	v_lshl_add_u64 v[90:91], v[142:143], 0, s[34:35]
	v_lshl_add_u64 v[92:93], v[90:91], 2, s[10:11]
	s_waitcnt vmcnt(22)
; #define LAS __attribute__((address_space(3)))
; DI unsigned pk2(float lo, float hi) { f32x2 v = {lo, hi}; bf16x2_t b = __builtin_convertvector(v, bf16x2_t); return __builtin_bit_cast(unsigned, b); }
;     DI void operator()(const f32x4 (&acc)[2][2][4][2], const Unit& u, int wr, int wc, int fr, int fq, const LAS unsigned char* slot) const {
;     ...
;         for (int ai = 0; ai < 2; ++ai)
; #pragma unroll
;             for (int m = 0; m < 4; ++m) { const size_t off = (size_t)(row0 + ai * HALF + m * 16) * D + col0; const float rs = *(const LAS float*)(slot + 4 * (ai * HALF + wr * 64 + m * 16 + fr));
; #pragma unroll
;                 for (int bj = 0; bj < 2; ++bj)
; #pragma unroll
;                     for (int n = 0; n < 2; ++n) { const f32x4 xv = *(const f32x4*)(x + off + bj * HALF + n * 16); const i32x4 ia = __builtin_bit_cast(i32x4, acc[ai][bj][m][n]);
;                         const f32x4 af = {(float)ia[0], (float)ia[1], (float)ia[2], (float)ia[3]};
;                         const f32x4 r = xv + (mv[bj][n] * rs) * af; *(u32x2*)(X1 + off + bj * HALF + n * 16) = (u32x2){pk2(r[0], r[1]), pk2(r[2], r[3])}; } }
	v_pk_fma_f32 v[84:85], v[94:95], v[84:85], v[238:239]
	v_pk_fma_f32 v[82:83], v[96:97], v[82:83], v[236:237]
	v_mov_b32_e32 v88, v103
	v_cvt_pk_bf16_f32 v82, v82, v83
	v_cvt_pk_bf16_f32 v83, v84, v85
	global_store_dwordx2 v[104:105], v[82:83], off offset:288
	global_load_dwordx4 v[236:239], v[248:249], off offset:576
	v_lshl_add_u64 v[86:87], v[90:91], 1, s[20:21]
	v_pk_mul_f32 v[90:91], v[126:127], v[88:89] op_sel_hi:[1,0]
	v_pk_mul_f32 v[94:95], v[128:129], v[88:89] op_sel_hi:[1,0]
	s_waitcnt vmcnt(22)
	v_pk_fma_f32 v[80:81], v[90:91], v[80:81], v[194:195]
	v_pk_fma_f32 v[78:79], v[94:95], v[78:79], v[192:193]
	v_pk_mul_f32 v[82:83], v[122:123], v[88:89] op_sel_hi:[1,0]
	v_cvt_pk_bf16_f32 v78, v78, v79
	v_cvt_pk_bf16_f32 v79, v80, v81
	global_store_dwordx2 v[86:87], v[78:79], off
	global_load_dwordx4 v[192:195], v[250:251], off
	v_pk_mul_f32 v[84:85], v[124:125], v[88:89] op_sel_hi:[1,0]
	s_waitcnt vmcnt(22)
	v_pk_fma_f32 v[76:77], v[82:83], v[76:77], v[198:199]
	v_pk_fma_f32 v[74:75], v[84:85], v[74:75], v[196:197]
	v_pk_mul_f32 v[78:79], v[118:119], v[88:89] op_sel_hi:[1,0]
	v_cvt_pk_bf16_f32 v74, v74, v75
	v_cvt_pk_bf16_f32 v75, v76, v77
	global_store_dwordx2 v[86:87], v[74:75], off offset:32
	global_load_dwordx4 v[196:199], v[250:251], off offset:64
	v_pk_mul_f32 v[80:81], v[120:121], v[88:89] op_sel_hi:[1,0]
	s_waitcnt vmcnt(22)
	v_pk_fma_f32 v[72:73], v[78:79], v[72:73], v[202:203]
	v_pk_fma_f32 v[70:71], v[80:81], v[70:71], v[200:201]
	v_pk_mul_f32 v[78:79], v[114:115], v[88:89] op_sel_hi:[1,0]
	v_cvt_pk_bf16_f32 v70, v70, v71
	v_cvt_pk_bf16_f32 v71, v72, v73
	global_store_dwordx2 v[86:87], v[70:71], off offset:256
	global_load_dwordx4 v[200:203], v[250:251], off offset:512
	v_pk_mul_f32 v[80:81], v[116:117], v[88:89] op_sel_hi:[1,0]
	v_lshl_add_u64 v[74:75], v[142:143], 0, s[16:17]
	v_lshl_add_u64 v[76:77], v[74:75], 2, s[10:11]
	s_waitcnt vmcnt(22)
	v_pk_fma_f32 v[68:69], v[78:79], v[68:69], v[206:207]
	v_pk_fma_f32 v[66:67], v[80:81], v[66:67], v[204:205]
	ds_read2_b32 v[70:71], v134 offset0:128 offset1:144
	v_cvt_pk_bf16_f32 v66, v66, v67
	v_cvt_pk_bf16_f32 v67, v68, v69
	global_store_dwordx2 v[86:87], v[66:67], off offset:288
	global_load_dwordx4 v[204:207], v[250:251], off offset:576
	v_lshl_add_u64 v[72:73], v[74:75], 1, s[20:21]
	s_waitcnt lgkmcnt(0)
	v_pk_mul_f32 v[74:75], v[126:127], v[70:71] op_sel_hi:[1,0]
	v_pk_mul_f32 v[78:79], v[128:129], v[70:71] op_sel_hi:[1,0]
	s_waitcnt vmcnt(22)
	v_pk_fma_f32 v[64:65], v[74:75], v[64:65], v[210:211]
	v_pk_fma_f32 v[62:63], v[78:79], v[62:63], v[208:209]
	v_pk_mul_f32 v[66:67], v[122:123], v[70:71] op_sel_hi:[1,0]
	v_cvt_pk_bf16_f32 v62, v62, v63
	v_cvt_pk_bf16_f32 v63, v64, v65
	global_store_dwordx2 v[72:73], v[62:63], off
	global_load_dwordx4 v[208:211], v[252:253], off
	v_pk_mul_f32 v[68:69], v[124:125], v[70:71] op_sel_hi:[1,0]
	s_waitcnt vmcnt(22)
	v_pk_fma_f32 v[60:61], v[66:67], v[60:61], v[214:215]
	v_pk_fma_f32 v[58:59], v[68:69], v[58:59], v[212:213]
	v_pk_mul_f32 v[62:63], v[118:119], v[70:71] op_sel_hi:[1,0]
	v_cvt_pk_bf16_f32 v58, v58, v59
	v_cvt_pk_bf16_f32 v59, v60, v61
	global_store_dwordx2 v[72:73], v[58:59], off offset:32
	global_load_dwordx4 v[212:215], v[252:253], off offset:64
	v_pk_mul_f32 v[64:65], v[120:121], v[70:71] op_sel_hi:[1,0]
	s_waitcnt vmcnt(22)
	v_pk_fma_f32 v[56:57], v[62:63], v[56:57], v[218:219]
	v_pk_fma_f32 v[54:55], v[64:65], v[54:55], v[216:217]
	v_pk_mul_f32 v[62:63], v[114:115], v[70:71] op_sel_hi:[1,0]
	v_cvt_pk_bf16_f32 v54, v54, v55
	v_cvt_pk_bf16_f32 v55, v56, v57
	global_store_dwordx2 v[72:73], v[54:55], off offset:256
	global_load_dwordx4 v[216:219], v[252:253], off offset:512
	v_pk_mul_f32 v[64:65], v[116:117], v[70:71] op_sel_hi:[1,0]
	v_lshl_add_u64 v[58:59], v[142:143], 0, s[36:37]
	v_lshl_add_u64 v[60:61], v[58:59], 2, s[10:11]
	s_waitcnt vmcnt(22)
	v_pk_fma_f32 v[52:53], v[62:63], v[52:53], v[222:223]
	v_pk_fma_f32 v[50:51], v[64:65], v[50:51], v[220:221]
	v_mov_b32_e32 v56, v71
	v_cvt_pk_bf16_f32 v50, v50, v51
	v_cvt_pk_bf16_f32 v51, v52, v53
	global_store_dwordx2 v[72:73], v[50:51], off offset:288
	global_load_dwordx4 v[220:223], v[252:253], off offset:576
	v_lshl_add_u64 v[54:55], v[58:59], 1, s[20:21]
	v_pk_mul_f32 v[58:59], v[126:127], v[56:57] op_sel_hi:[1,0]
	v_pk_mul_f32 v[62:63], v[128:129], v[56:57] op_sel_hi:[1,0]
	s_waitcnt vmcnt(22)
	v_pk_fma_f32 v[48:49], v[58:59], v[48:49], v[226:227]
	v_pk_fma_f32 v[46:47], v[62:63], v[46:47], v[224:225]
	v_pk_mul_f32 v[50:51], v[122:123], v[56:57] op_sel_hi:[1,0]
	v_cvt_pk_bf16_f32 v46, v46, v47
	v_cvt_pk_bf16_f32 v47, v48, v49
	global_store_dwordx2 v[54:55], v[46:47], off
	v_pk_mul_f32 v[52:53], v[124:125], v[56:57] op_sel_hi:[1,0]
	s_waitcnt vmcnt(21)
	v_pk_fma_f32 v[44:45], v[50:51], v[44:45], v[230:231]
	v_pk_fma_f32 v[42:43], v[52:53], v[42:43], v[228:229]
	v_pk_mul_f32 v[46:47], v[118:119], v[56:57] op_sel_hi:[1,0]
	v_cvt_pk_bf16_f32 v42, v42, v43
	v_cvt_pk_bf16_f32 v43, v44, v45
	global_store_dwordx2 v[54:55], v[42:43], off offset:32
	v_pk_mul_f32 v[48:49], v[120:121], v[56:57] op_sel_hi:[1,0]
	s_waitcnt vmcnt(20)
; #define LAS __attribute__((address_space(3)))
; DI unsigned pk2(float lo, float hi) { f32x2 v = {lo, hi}; bf16x2_t b = __builtin_convertvector(v, bf16x2_t); return __builtin_bit_cast(unsigned, b); }
; #define PG8_BAR __builtin_amdgcn_s_barrier()
;     ...
;         cur = nxt; cB = nB; ++ui;
;         E.prefetch(cur, xep + (ui & 1) * 4096, wid, lane);
; #pragma unroll
;         for (int i = 0; i < 2; ++i) { ao0[i] = no0[i]; ao1[i] = no1[i]; }
;         if constexpr (ALIGN_EPI) { if (wr == 1) PG8_BAR; }
;     DI void operator()(const f32x4 (&acc)[2][2][4][2], const Unit& u, int wr, int wc, int fr, int fq, const LAS unsigned char* slot) const {
;     ...
;         for (int ai = 0; ai < 2; ++ai)
; #pragma unroll
;             for (int m = 0; m < 4; ++m) { const size_t off = (size_t)(row0 + ai * HALF + m * 16) * D + col0; const float rs = *(const LAS float*)(slot + 4 * (ai * HALF + wr * 64 + m * 16 + fr));
; #pragma unroll
;                 for (int bj = 0; bj < 2; ++bj)
; #pragma unroll
;                     for (int n = 0; n < 2; ++n) { const f32x4 xv = *(const f32x4*)(x + off + bj * HALF + n * 16); const i32x4 ia = __builtin_bit_cast(i32x4, acc[ai][bj][m][n]);
;                         const f32x4 af = {(float)ia[0], (float)ia[1], (float)ia[2], (float)ia[3]};
;                         const f32x4 r = xv + (mv[bj][n] * rs) * af; *(u32x2*)(X1 + off + bj * HALF + n * 16) = (u32x2){pk2(r[0], r[1]), pk2(r[2], r[3])}; } }
	v_pk_fma_f32 v[36:37], v[46:47], v[36:37], v[234:235]
	v_pk_fma_f32 v[34:35], v[48:49], v[34:35], v[232:233]
	v_pk_mul_f32 v[46:47], v[114:115], v[56:57] op_sel_hi:[1,0]
	v_cvt_pk_bf16_f32 v34, v34, v35
	v_cvt_pk_bf16_f32 v35, v36, v37
	global_store_dwordx2 v[54:55], v[34:35], off offset:256
	v_pk_mul_f32 v[48:49], v[116:117], v[56:57] op_sel_hi:[1,0]
	v_lshl_add_u64 v[42:43], v[142:143], 0, s[38:39]
	v_lshl_add_u64 v[44:45], v[42:43], 2, s[10:11]
	s_waitcnt vmcnt(19)
	v_pk_fma_f32 v[24:25], v[46:47], v[24:25], v[238:239]
	v_pk_fma_f32 v[22:23], v[48:49], v[22:23], v[236:237]
	ds_read2_b32 v[34:35], v134 offset0:160 offset1:176
	v_cvt_pk_bf16_f32 v22, v22, v23
	v_cvt_pk_bf16_f32 v23, v24, v25
	global_store_dwordx2 v[54:55], v[22:23], off offset:288
	v_lshl_add_u64 v[36:37], v[42:43], 1, s[20:21]
	s_waitcnt lgkmcnt(0)
	v_pk_mul_f32 v[42:43], v[126:127], v[34:35] op_sel_hi:[1,0]
	v_pk_mul_f32 v[46:47], v[128:129], v[34:35] op_sel_hi:[1,0]
	s_waitcnt vmcnt(18)
	v_pk_fma_f32 v[24:25], v[42:43], v[28:29], v[194:195]
	v_pk_fma_f32 v[22:23], v[46:47], v[26:27], v[192:193]
	v_pk_mul_f32 v[26:27], v[122:123], v[34:35] op_sel_hi:[1,0]
	v_cvt_pk_bf16_f32 v22, v22, v23
	v_cvt_pk_bf16_f32 v23, v24, v25
	global_store_dwordx2 v[36:37], v[22:23], off
	v_pk_mul_f32 v[28:29], v[124:125], v[34:35] op_sel_hi:[1,0]
	s_waitcnt vmcnt(17)
	v_pk_fma_f32 v[20:21], v[26:27], v[20:21], v[198:199]
	v_pk_fma_f32 v[18:19], v[28:29], v[18:19], v[196:197]
	v_cvt_f32_i32_e32 v23, v39
	v_cvt_pk_bf16_f32 v18, v18, v19
	v_cvt_pk_bf16_f32 v19, v20, v21
	global_store_dwordx2 v[36:37], v[18:19], off offset:32
	v_cvt_f32_i32_e32 v25, v41
	v_cvt_f32_i32_e32 v24, v40
	v_cvt_f32_i32_e32 v22, v38
	v_pk_mul_f32 v[26:27], v[118:119], v[34:35] op_sel_hi:[1,0]
	v_pk_mul_f32 v[28:29], v[120:121], v[34:35] op_sel_hi:[1,0]
	s_waitcnt vmcnt(16)
	v_pk_fma_f32 v[20:21], v[26:27], v[24:25], v[202:203]
	v_pk_fma_f32 v[18:19], v[28:29], v[22:23], v[200:201]
	v_cvt_f32_i32_e32 v23, v31
	v_cvt_pk_bf16_f32 v18, v18, v19
	v_cvt_pk_bf16_f32 v19, v20, v21
	global_store_dwordx2 v[36:37], v[18:19], off offset:256
	v_cvt_f32_i32_e32 v22, v30
	v_cvt_f32_i32_e32 v25, v33
	v_cvt_f32_i32_e32 v24, v32
	v_pk_mul_f32 v[30:31], v[114:115], v[34:35] op_sel_hi:[1,0]
	v_pk_mul_f32 v[32:33], v[116:117], v[34:35] op_sel_hi:[1,0]
	v_lshl_add_u64 v[26:27], v[142:143], 0, s[42:43]
	v_lshl_add_u64 v[28:29], v[26:27], 2, s[10:11]
	s_waitcnt vmcnt(15)
	v_pk_fma_f32 v[20:21], v[30:31], v[24:25], v[206:207]
	v_pk_fma_f32 v[18:19], v[32:33], v[22:23], v[204:205]
	v_mov_b32_e32 v24, v35
	v_cvt_pk_bf16_f32 v18, v18, v19
	v_cvt_pk_bf16_f32 v19, v20, v21
	global_store_dwordx2 v[36:37], v[18:19], off offset:288
	v_lshl_add_u64 v[22:23], v[26:27], 1, s[20:21]
	v_pk_mul_f32 v[26:27], v[126:127], v[24:25] op_sel_hi:[1,0]
	v_pk_mul_f32 v[30:31], v[128:129], v[24:25] op_sel_hi:[1,0]
	s_waitcnt vmcnt(14)
	v_pk_fma_f32 v[8:9], v[26:27], v[8:9], v[210:211]
	v_pk_fma_f32 v[6:7], v[30:31], v[6:7], v[208:209]
	v_pk_mul_f32 v[18:19], v[122:123], v[24:25] op_sel_hi:[1,0]
	v_cvt_pk_bf16_f32 v6, v6, v7
	v_cvt_pk_bf16_f32 v7, v8, v9
	global_store_dwordx2 v[22:23], v[6:7], off
	v_pk_mul_f32 v[20:21], v[124:125], v[24:25] op_sel_hi:[1,0]
	s_waitcnt vmcnt(13)
	v_pk_fma_f32 v[4:5], v[18:19], v[4:5], v[214:215]
	v_pk_fma_f32 v[2:3], v[20:21], v[2:3], v[212:213]
	v_cvt_f32_i32_e32 v7, v15
	v_cvt_pk_bf16_f32 v2, v2, v3
	v_cvt_pk_bf16_f32 v3, v4, v5
	global_store_dwordx2 v[22:23], v[2:3], off offset:32
	v_cvt_f32_i32_e32 v9, v17
	v_cvt_f32_i32_e32 v8, v16
	v_cvt_f32_i32_e32 v6, v14
	v_pk_mul_f32 v[14:15], v[118:119], v[24:25] op_sel_hi:[1,0]
	v_pk_mul_f32 v[16:17], v[120:121], v[24:25] op_sel_hi:[1,0]
	s_waitcnt vmcnt(12)
	v_pk_fma_f32 v[4:5], v[14:15], v[8:9], v[218:219]
	v_pk_fma_f32 v[2:3], v[16:17], v[6:7], v[216:217]
	v_cvt_f32_i32_e32 v7, v11
	v_cvt_pk_bf16_f32 v2, v2, v3
	v_cvt_pk_bf16_f32 v3, v4, v5
	global_store_dwordx2 v[22:23], v[2:3], off offset:256
	v_cvt_f32_i32_e32 v6, v10
	v_cvt_f32_i32_e32 v9, v13
	v_cvt_f32_i32_e32 v8, v12
	v_pk_mul_f32 v[10:11], v[114:115], v[24:25] op_sel_hi:[1,0]
	v_pk_mul_f32 v[12:13], v[116:117], v[24:25] op_sel_hi:[1,0]
	s_waitcnt vmcnt(11)
	v_pk_fma_f32 v[4:5], v[10:11], v[8:9], v[222:223]
	v_pk_fma_f32 v[2:3], v[12:13], v[6:7], v[220:221]
	s_nop 0
	v_cvt_pk_bf16_f32 v2, v2, v3
	v_cvt_pk_bf16_f32 v3, v4, v5
	global_store_dwordx2 v[22:23], v[2:3], off offset:288
	s_cbranch_vccnz .LBB0_1633
	s_andn2_b64 vcc, exec, s[12:13]
	s_add_i32 s74, s74, 1
	s_cbranch_vccnz .LBB0_1659
	s_lshl_b32 s4, s74, 12
	s_and_b32 s4, s4, 0x1000
	s_add_i32 s54, s4, 0
	s_lshl_b32 s4, s77, 8
	s_ashr_i32 s5, s4, 31
	v_lshl_add_u64 v[2:3], s[4:5], 2, v[136:137]
	s_lshl_b32 s4, s76, 8
	s_ashr_i32 s5, s4, 31
	s_add_i32 m0, s54, 0x21000
	s_lshl_b64 s[4:5], s[4:5], 2
	global_load_lds_dwordx4 v[2:3], off
	v_lshl_add_u64 v[2:3], v[138:139], 0, s[4:5]
	s_add_i32 m0, s54, 0x21400
	s_nop 0
	global_load_lds_dwordx4 v[2:3], off
	v_lshl_add_u64 v[2:3], v[140:141], 0, s[4:5]
	s_add_i32 m0, s54, 0x21800
	s_nop 0
	global_load_lds_dwordx4 v[2:3], off
